# fused LSTM: recurrent product on two accumulators with half-masked B operands (4 LDS reads), one 4-DPP merge instead of 12
# speedup vs baseline: 1.0044x; 1.0044x over previous
_Z12lstm2_kernelPKDF16_PKDv8_DF16_Pf:
	s_load_dwordx4 s[8:11], s[0:1], 0x0
	s_load_dwordx2 s[12:13], s[0:1], 0x10
	s_and_b32 s14, s2, 1
	s_lshr_b32 s15, s2, 1
	v_and_b32_e32 v1, 63, v0
	v_lshrrev_b32_e32 v2, 6, v0
	v_lshrrev_b32_e32 v3, 4, v1
	v_and_b32_e32 v4, 15, v0
	v_lshrrev_b32_e32 v5, 2, v4
	v_and_b32_e32 v6, 3, v0
	v_lshlrev_b32_e32 v7, 4, v1
	v_lshl_add_u32 v8, v2, 13, v7
	v_lshl_add_u32 v9, v2, 14, v7
	s_waitcnt lgkmcnt(0)
	s_lshl_b32 s16, s14, 15
	s_add_u32 s16, s16, 0x64000
	s_add_u32 s16, s10, s16
	s_addc_u32 s17, s11, 0
	s_lshl_b32 s18, s14, 16
	s_add_u32 s18, s18, 0x44000
	s_add_u32 s18, s10, s18
	s_addc_u32 s19, s11, 0
	v_add_u32_e32 v10, 0x1000, v8
	global_load_dwordx4 v[16:19], v8, s[16:17] offset:0
	global_load_dwordx4 v[20:23], v8, s[16:17] offset:1024
	global_load_dwordx4 v[24:27], v8, s[16:17] offset:2048
	global_load_dwordx4 v[28:31], v8, s[16:17] offset:3072
	global_load_dwordx4 v[32:35], v10, s[16:17] offset:0
	global_load_dwordx4 v[36:39], v10, s[16:17] offset:1024
	global_load_dwordx4 v[40:43], v10, s[16:17] offset:2048
	global_load_dwordx4 v[44:47], v10, s[16:17] offset:3072
	v_add_u32_e32 v11, 0x1000, v9
	v_add_u32_e32 v12, 0x2000, v9
	v_add_u32_e32 v13, 0x3000, v9
	global_load_dwordx4 v[48:51], v9, s[18:19] offset:0
	global_load_dwordx4 v[52:55], v9, s[18:19] offset:1024
	global_load_dwordx4 v[56:59], v9, s[18:19] offset:2048
	global_load_dwordx4 v[60:63], v9, s[18:19] offset:3072
	global_load_dwordx4 v[64:67], v11, s[18:19] offset:0
	global_load_dwordx4 v[68:71], v11, s[18:19] offset:1024
	global_load_dwordx4 v[72:75], v11, s[18:19] offset:2048
	global_load_dwordx4 v[76:79], v11, s[18:19] offset:3072
	global_load_dwordx4 v[80:83], v12, s[18:19] offset:0
	global_load_dwordx4 v[84:87], v12, s[18:19] offset:1024
	global_load_dwordx4 v[88:91], v12, s[18:19] offset:2048
	global_load_dwordx4 v[92:95], v12, s[18:19] offset:3072
	global_load_dwordx4 v[96:99], v13, s[18:19] offset:0
	global_load_dwordx4 v[100:103], v13, s[18:19] offset:1024
	global_load_dwordx4 v[104:107], v13, s[18:19] offset:2048
	global_load_dwordx4 v[108:111], v13, s[18:19] offset:3072
	s_lshl_b32 s22, s14, 10
	s_add_u32 s22, s8, s22
	s_addc_u32 s23, s9, 0
	v_lshl_add_u32 v14, v2, 4, v3
	v_lshlrev_b32_e32 v14, 2, v14
	global_load_dword v112, v14, s[22:23] offset:0
	global_load_dword v113, v14, s[22:23] offset:256
	global_load_dword v114, v14, s[22:23] offset:512
	global_load_dword v115, v14, s[22:23] offset:768
	global_load_dword v116, v14, s[22:23] offset:16
	global_load_dword v117, v14, s[22:23] offset:272
	global_load_dword v118, v14, s[22:23] offset:528
	global_load_dword v119, v14, s[22:23] offset:784
	global_load_dword v120, v14, s[22:23] offset:32
	global_load_dword v121, v14, s[22:23] offset:288
	global_load_dword v122, v14, s[22:23] offset:544
	global_load_dword v123, v14, s[22:23] offset:800
	global_load_dword v124, v14, s[22:23] offset:48
	global_load_dword v125, v14, s[22:23] offset:304
	global_load_dword v126, v14, s[22:23] offset:560
	global_load_dword v127, v14, s[22:23] offset:816
	s_add_u32 s24, s8, 0xc808000
	s_addc_u32 s25, s9, 0
	s_lshl_b32 s26, s15, 2
	v_add_u32_e32 v15, s26, v6
	s_cmp_eq_u32 s14, 0
	v_sub_u32_e32 v200, 0x18f, v5
	s_cselect_b64 vcc, -1, 0
	s_nop 1
	v_cndmask_b32_e32 v200, v200, v5, vcc
	v_mov_b32_e32 v201, 0x190
	v_mad_u32_u24 v200, v15, v201, v200
	v_lshlrev_b32_e32 v200, 8, v200
	v_lshl_add_u32 v200, v3, 4, v200
	v_mov_b32_e32 v201, 0
	v_lshl_add_u64 v[228:229], s[24:25], 0, v[200:201]
	s_mov_b32 s28, 0x400
	s_cselect_b32 s20, s28, 0xfffffc00
	s_cselect_b32 s21, 0, -1
	global_load_dwordx4 v[128:131], v[228:229], off offset:0
	global_load_dwordx4 v[132:135], v[228:229], off offset:64
	global_load_dwordx4 v[136:139], v[228:229], off offset:128
	global_load_dwordx4 v[140:143], v[228:229], off offset:192
	v_lshl_add_u64 v[228:229], v[228:229], 0, s[20:21]
	global_load_dwordx4 v[144:147], v[228:229], off offset:0
	global_load_dwordx4 v[148:151], v[228:229], off offset:64
	global_load_dwordx4 v[152:155], v[228:229], off offset:128
	global_load_dwordx4 v[156:159], v[228:229], off offset:192
	v_lshl_add_u64 v[228:229], v[228:229], 0, s[20:21]
	v_mul_u32_u24_e32 v202, 144, v6
	v_lshl_add_u32 v224, v3, 4, v202
	v_lshl_add_u32 v203, v2, 4, v3
	v_lshl_add_u32 v203, v5, 2, v203
	v_lshl_add_u32 v225, v203, 1, v202
	v_mul_u32_u24_e32 v204, 8704, v2
	v_lshlrev_b32_e32 v205, 8, v3
	v_lshl_add_u32 v205, v6, 4, v205
	v_add_u32_e32 v205, 1280, v205
	v_add_u32_e32 v205, v205, v204
	v_lshl_add_u32 v226, v5, 6, v205
	v_mul_u32_u24_e32 v206, 1088, v5
	v_add_u32_e32 v227, v205, v206
	v_lshlrev_b32_e32 v206, 4, v3
	v_cmp_gt_u32_e32 vcc, 2, v5
	s_nop 1
	v_add_u32_e32 v208, 1152, v206
	v_cndmask_b32_e32 v209, v208, v224, vcc
	v_cndmask_b32_e32 v211, v224, v208, vcc
	v_add_u32_e32 v208, 576, v206
	v_cndmask_b32_e32 v210, v208, v224, vcc
	v_cndmask_b32_e32 v212, v224, v208, vcc
	s_lshl_b32 s27, s14, 6
	v_lshl_add_u32 v230, v15, 7, v203
	v_add_u32_e32 v230, s27, v230
	v_lshlrev_b32_e32 v230, 2, v230
	v_mov_b32_e32 v208, 0
	v_lshlrev_b32_e32 v200, 2, v0
	v_lshlrev_b32_e32 v201, 2, v1
	ds_write_b32 v200, v208
	ds_write_b32 v201, v208 offset:1024
	v_mov_b32_e32 v220, 0
	v_mov_b32_e32 v221, 0xff61b1e6
	v_mov_b32_e32 v222, 0x4038aa3b
	v_mov_b32_e32 v215, 0xff61b1e6
	s_waitcnt vmcnt(0)
	v_mfma_f32_16x16x32_f16 v[168:171], v[48:51], v[128:131], v[112:115]
	v_mfma_f32_16x16x32_f16 v[168:171], v[52:55], v[132:135], v[168:171]
	v_mfma_f32_16x16x32_f16 v[168:171], v[56:59], v[136:139], v[168:171]
	v_mfma_f32_16x16x32_f16 v[168:171], v[60:63], v[140:143], v[168:171]
	v_mfma_f32_16x16x32_f16 v[172:175], v[64:67], v[128:131], v[116:119]
	v_mfma_f32_16x16x32_f16 v[172:175], v[68:71], v[132:135], v[172:175]
	v_mfma_f32_16x16x32_f16 v[172:175], v[72:75], v[136:139], v[172:175]
	v_mfma_f32_16x16x32_f16 v[172:175], v[76:79], v[140:143], v[172:175]
	v_mfma_f32_16x16x32_f16 v[176:179], v[80:83], v[128:131], v[120:123]
	v_mfma_f32_16x16x32_f16 v[176:179], v[84:87], v[132:135], v[176:179]
	v_mfma_f32_16x16x32_f16 v[176:179], v[88:91], v[136:139], v[176:179]
	v_mfma_f32_16x16x32_f16 v[176:179], v[92:95], v[140:143], v[176:179]
	v_mfma_f32_16x16x32_f16 v[180:183], v[96:99], v[128:131], v[124:127]
	v_mfma_f32_16x16x32_f16 v[180:183], v[100:103], v[132:135], v[180:183]
	v_mfma_f32_16x16x32_f16 v[180:183], v[104:107], v[136:139], v[180:183]
	v_mfma_f32_16x16x32_f16 v[180:183], v[108:111], v[140:143], v[180:183]
	v_mfma_f32_16x16x32_f16 v[160:163], v[48:51], v[144:147], v[112:115]
	v_mfma_f32_16x16x32_f16 v[164:167], v[64:67], v[144:147], v[116:119]
	v_mfma_f32_16x16x32_f16 v[160:163], v[52:55], v[148:151], v[160:163]
	v_mfma_f32_16x16x32_f16 v[160:163], v[56:59], v[152:155], v[160:163]
	s_nop 7
	ds_write_b128 v227, v[168:171] offset:0
	ds_write_b128 v227, v[172:175] offset:64
	ds_write_b128 v227, v[176:179] offset:128
	ds_write_b128 v227, v[180:183] offset:192
	s_movk_i32 s4, 50
	s_waitcnt lgkmcnt(0)
	s_barrier
	ds_read_b128 v[192:195], v226 offset:0
.Llstm3_loop:
	ds_read_b128 v[184:187], v209 offset:0
	ds_read_b128 v[188:191], v209 offset:64
	ds_read_b128 v[176:179], v211 offset:0
	ds_read_b128 v[180:183], v211 offset:64
	v_mfma_f32_16x16x32_f16 v[164:167], v[68:71], v[148:151], v[164:167]
	v_mfma_f32_16x16x32_f16 v[160:163], v[60:63], v[156:159], v[160:163]
	global_load_dwordx4 v[128:131], v[228:229], off offset:0
	global_load_dwordx4 v[132:135], v[228:229], off offset:64
	global_load_dwordx4 v[136:139], v[228:229], off offset:128
	global_load_dwordx4 v[140:143], v[228:229], off offset:192
	v_lshl_add_u64 v[228:229], v[228:229], 0, s[20:21]
	s_waitcnt lgkmcnt(3)
	v_mfma_f32_16x16x32_f16 v[168:171], v[16:19], v[184:187], v[192:195]
	v_mfma_f32_16x16x32_f16 v[172:175], v[24:27], v[184:187], v[192:195]
	s_waitcnt lgkmcnt(2)
	v_mfma_f32_16x16x32_f16 v[168:171], v[20:23], v[188:191], v[168:171]
	v_mfma_f32_16x16x32_f16 v[172:175], v[28:31], v[188:191], v[172:175]
	s_waitcnt lgkmcnt(1)
	v_mfma_f32_16x16x32_f16 v[168:171], v[32:35], v[176:179], v[168:171]
	v_mfma_f32_16x16x32_f16 v[172:175], v[40:43], v[176:179], v[172:175]
	s_waitcnt lgkmcnt(0)
	v_mfma_f32_16x16x32_f16 v[168:171], v[36:39], v[180:183], v[168:171]
	v_mfma_f32_16x16x32_f16 v[172:175], v[44:47], v[180:183], v[172:175]
	v_max_f32_e32 v221, v221, v215
	s_nop 6
	v_mov_b32_dpp v168, v172 quad_perm:[0,1,2,3] row_mask:0xf bank_mask:0xa
	v_mov_b32_dpp v169, v173 quad_perm:[0,1,2,3] row_mask:0xf bank_mask:0xa
	v_mov_b32_dpp v170, v174 quad_perm:[0,1,2,3] row_mask:0xf bank_mask:0xa
	v_exp_f32_e32 v200, v168
	v_mov_b32_dpp v171, v175 quad_perm:[0,1,2,3] row_mask:0xf bank_mask:0xa
	v_exp_f32_e32 v201, v169
	v_exp_f32_e32 v202, v170
	v_add_f32_e32 v200, 1.0, v200
	v_exp_f32_e32 v203, v171
	v_add_f32_e32 v201, 1.0, v201
	v_add_f32_e32 v202, 1.0, v202
	v_rcp_f32_e32 v202, v202
	v_rcp_f32_e32 v200, v200
	v_rcp_f32_e32 v201, v201
	v_add_f32_e32 v203, 1.0, v203
	v_fmamk_f32 v204, v202, 0xc0b8aa3b, v222
	v_rcp_f32_e32 v203, v203
	v_mul_f32_e32 v205, v200, v204
	v_fma_f32 v220, v201, v220, v205
	v_exp_f32_e32 v206, v220
	v_mul_f32_e32 v207, -2.0, v203
	v_add_f32_e32 v206, 1.0, v206
	v_rcp_f32_e32 v206, v206
	s_nop 0
	v_fma_mixlo_f16 v208, v206, v207, v203
	ds_write_b16 v225, v208 offset:576
	v_fma_f32 v215, v206, v207, v203
	v_mfma_f32_16x16x32_f16 v[232:235], v[80:83], v[144:147], v[120:123]
	v_mfma_f32_16x16x32_f16 v[164:167], v[72:75], v[152:155], v[164:167]
	ds_write_b128 v227, v[160:163] offset:4352
	ds_read_b128 v[196:199], v226 offset:1088
	s_waitcnt lgkmcnt(2)
	s_barrier
	ds_read_b128 v[184:187], v210 offset:576
	ds_read_b128 v[188:191], v210 offset:640
	ds_read_b128 v[176:179], v212 offset:576
	ds_read_b128 v[180:183], v212 offset:640
	v_mfma_f32_16x16x32_f16 v[232:235], v[84:87], v[148:151], v[232:235]
	v_mfma_f32_16x16x32_f16 v[164:167], v[76:79], v[156:159], v[164:167]
	s_waitcnt lgkmcnt(3)
	v_mfma_f32_16x16x32_f16 v[168:171], v[16:19], v[184:187], v[196:199]
	v_mfma_f32_16x16x32_f16 v[172:175], v[24:27], v[184:187], v[196:199]
	s_waitcnt lgkmcnt(2)
	v_mfma_f32_16x16x32_f16 v[168:171], v[20:23], v[188:191], v[168:171]
	v_mfma_f32_16x16x32_f16 v[172:175], v[28:31], v[188:191], v[172:175]
	s_waitcnt lgkmcnt(1)
	v_mfma_f32_16x16x32_f16 v[168:171], v[32:35], v[176:179], v[168:171]
	v_mfma_f32_16x16x32_f16 v[172:175], v[40:43], v[176:179], v[172:175]
	s_waitcnt lgkmcnt(0)
	v_mfma_f32_16x16x32_f16 v[168:171], v[36:39], v[180:183], v[168:171]
	v_mfma_f32_16x16x32_f16 v[172:175], v[44:47], v[180:183], v[172:175]
	v_max_f32_e32 v221, v221, v215
	s_nop 6
	v_mov_b32_dpp v168, v172 quad_perm:[0,1,2,3] row_mask:0xf bank_mask:0xa
	v_mov_b32_dpp v169, v173 quad_perm:[0,1,2,3] row_mask:0xf bank_mask:0xa
	v_mov_b32_dpp v170, v174 quad_perm:[0,1,2,3] row_mask:0xf bank_mask:0xa
	v_exp_f32_e32 v200, v168
	v_mov_b32_dpp v171, v175 quad_perm:[0,1,2,3] row_mask:0xf bank_mask:0xa
	v_exp_f32_e32 v201, v169
	v_exp_f32_e32 v202, v170
	v_add_f32_e32 v200, 1.0, v200
	v_exp_f32_e32 v203, v171
	v_add_f32_e32 v201, 1.0, v201
	v_add_f32_e32 v202, 1.0, v202
	v_rcp_f32_e32 v202, v202
	v_rcp_f32_e32 v200, v200
	v_rcp_f32_e32 v201, v201
	v_add_f32_e32 v203, 1.0, v203
	v_fmamk_f32 v204, v202, 0xc0b8aa3b, v222
	v_rcp_f32_e32 v203, v203
	v_mul_f32_e32 v205, v200, v204
	v_fma_f32 v220, v201, v220, v205
	v_exp_f32_e32 v206, v220
	v_mul_f32_e32 v207, -2.0, v203
	v_add_f32_e32 v206, 1.0, v206
	v_rcp_f32_e32 v206, v206
	s_nop 0
	v_fma_mixlo_f16 v208, v206, v207, v203
	ds_write_b16 v225, v208 offset:0
	v_fma_f32 v215, v206, v207, v203
	v_mfma_f32_16x16x32_f16 v[236:239], v[96:99], v[144:147], v[124:127]
	v_mfma_f32_16x16x32_f16 v[232:235], v[88:91], v[152:155], v[232:235]
	ds_write_b128 v227, v[164:167] offset:4416
	ds_read_b128 v[192:195], v226 offset:2176
	s_waitcnt lgkmcnt(2)
	s_barrier
	ds_read_b128 v[184:187], v209 offset:0
	ds_read_b128 v[188:191], v209 offset:64
	ds_read_b128 v[176:179], v211 offset:0
	ds_read_b128 v[180:183], v211 offset:64
	v_mfma_f32_16x16x32_f16 v[236:239], v[100:103], v[148:151], v[236:239]
	v_mfma_f32_16x16x32_f16 v[232:235], v[92:95], v[156:159], v[232:235]
	s_waitcnt lgkmcnt(3)
	v_mfma_f32_16x16x32_f16 v[168:171], v[16:19], v[184:187], v[192:195]
	v_mfma_f32_16x16x32_f16 v[172:175], v[24:27], v[184:187], v[192:195]
	s_waitcnt lgkmcnt(2)
	v_mfma_f32_16x16x32_f16 v[168:171], v[20:23], v[188:191], v[168:171]
	v_mfma_f32_16x16x32_f16 v[172:175], v[28:31], v[188:191], v[172:175]
	s_waitcnt lgkmcnt(1)
	v_mfma_f32_16x16x32_f16 v[168:171], v[32:35], v[176:179], v[168:171]
	v_mfma_f32_16x16x32_f16 v[172:175], v[40:43], v[176:179], v[172:175]
	s_waitcnt lgkmcnt(0)
	v_mfma_f32_16x16x32_f16 v[168:171], v[36:39], v[180:183], v[168:171]
	v_mfma_f32_16x16x32_f16 v[172:175], v[44:47], v[180:183], v[172:175]
	v_max_f32_e32 v221, v221, v215
	s_nop 6
	v_mov_b32_dpp v168, v172 quad_perm:[0,1,2,3] row_mask:0xf bank_mask:0xa
	v_mov_b32_dpp v169, v173 quad_perm:[0,1,2,3] row_mask:0xf bank_mask:0xa
	v_mov_b32_dpp v170, v174 quad_perm:[0,1,2,3] row_mask:0xf bank_mask:0xa
	v_exp_f32_e32 v200, v168
	v_mov_b32_dpp v171, v175 quad_perm:[0,1,2,3] row_mask:0xf bank_mask:0xa
	v_exp_f32_e32 v201, v169
	v_exp_f32_e32 v202, v170
	v_add_f32_e32 v200, 1.0, v200
	v_exp_f32_e32 v203, v171
	v_add_f32_e32 v201, 1.0, v201
	v_add_f32_e32 v202, 1.0, v202
	v_rcp_f32_e32 v202, v202
	v_rcp_f32_e32 v200, v200
	v_rcp_f32_e32 v201, v201
	v_add_f32_e32 v203, 1.0, v203
	v_fmamk_f32 v204, v202, 0xc0b8aa3b, v222
	v_rcp_f32_e32 v203, v203
	v_mul_f32_e32 v205, v200, v204
	v_fma_f32 v220, v201, v220, v205
	v_exp_f32_e32 v206, v220
	v_mul_f32_e32 v207, -2.0, v203
	v_add_f32_e32 v206, 1.0, v206
	v_rcp_f32_e32 v206, v206
	s_nop 0
	v_fma_mixlo_f16 v208, v206, v207, v203
	ds_write_b16 v225, v208 offset:576
	v_fma_f32 v215, v206, v207, v203
	s_waitcnt vmcnt(0)
	v_mfma_f32_16x16x32_f16 v[160:163], v[48:51], v[128:131], v[112:115]
	v_mfma_f32_16x16x32_f16 v[236:239], v[104:107], v[152:155], v[236:239]
	ds_write_b128 v227, v[232:235] offset:4480
	ds_read_b128 v[196:199], v226 offset:3264
	s_waitcnt lgkmcnt(2)
	s_barrier
	ds_read_b128 v[184:187], v210 offset:576
	ds_read_b128 v[188:191], v210 offset:640
	ds_read_b128 v[176:179], v212 offset:576
	ds_read_b128 v[180:183], v212 offset:640
	v_mfma_f32_16x16x32_f16 v[160:163], v[52:55], v[132:135], v[160:163]
	v_mfma_f32_16x16x32_f16 v[236:239], v[108:111], v[156:159], v[236:239]
	s_waitcnt lgkmcnt(3)
	v_mfma_f32_16x16x32_f16 v[168:171], v[16:19], v[184:187], v[196:199]
	v_mfma_f32_16x16x32_f16 v[172:175], v[24:27], v[184:187], v[196:199]
	s_waitcnt lgkmcnt(2)
	v_mfma_f32_16x16x32_f16 v[168:171], v[20:23], v[188:191], v[168:171]
	v_mfma_f32_16x16x32_f16 v[172:175], v[28:31], v[188:191], v[172:175]
	s_waitcnt lgkmcnt(1)
	v_mfma_f32_16x16x32_f16 v[168:171], v[32:35], v[176:179], v[168:171]
	v_mfma_f32_16x16x32_f16 v[172:175], v[40:43], v[176:179], v[172:175]
	s_waitcnt lgkmcnt(0)
	v_mfma_f32_16x16x32_f16 v[168:171], v[36:39], v[180:183], v[168:171]
	v_mfma_f32_16x16x32_f16 v[172:175], v[44:47], v[180:183], v[172:175]
	v_max_f32_e32 v221, v221, v215
	s_nop 6
	v_mov_b32_dpp v168, v172 quad_perm:[0,1,2,3] row_mask:0xf bank_mask:0xa
	v_mov_b32_dpp v169, v173 quad_perm:[0,1,2,3] row_mask:0xf bank_mask:0xa
	v_mov_b32_dpp v170, v174 quad_perm:[0,1,2,3] row_mask:0xf bank_mask:0xa
	v_exp_f32_e32 v200, v168
	v_mov_b32_dpp v171, v175 quad_perm:[0,1,2,3] row_mask:0xf bank_mask:0xa
	v_exp_f32_e32 v201, v169
	v_exp_f32_e32 v202, v170
	v_add_f32_e32 v200, 1.0, v200
	v_exp_f32_e32 v203, v171
	v_add_f32_e32 v201, 1.0, v201
	v_add_f32_e32 v202, 1.0, v202
	v_rcp_f32_e32 v202, v202
	v_rcp_f32_e32 v200, v200
	v_rcp_f32_e32 v201, v201
	v_add_f32_e32 v203, 1.0, v203
	v_fmamk_f32 v204, v202, 0xc0b8aa3b, v222
	v_rcp_f32_e32 v203, v203
	v_mul_f32_e32 v205, v200, v204
	v_fma_f32 v220, v201, v220, v205
	v_exp_f32_e32 v206, v220
	v_mul_f32_e32 v207, -2.0, v203
	v_add_f32_e32 v206, 1.0, v206
	v_rcp_f32_e32 v206, v206
	s_nop 0
	v_fma_mixlo_f16 v208, v206, v207, v203
	ds_write_b16 v225, v208 offset:0
	v_fma_f32 v215, v206, v207, v203
	v_mfma_f32_16x16x32_f16 v[164:167], v[64:67], v[128:131], v[116:119]
	v_mfma_f32_16x16x32_f16 v[160:163], v[56:59], v[136:139], v[160:163]
	ds_write_b128 v227, v[236:239] offset:4544
	ds_read_b128 v[192:195], v226 offset:4352
	s_waitcnt lgkmcnt(2)
	s_barrier
	ds_read_b128 v[184:187], v209 offset:0
	ds_read_b128 v[188:191], v209 offset:64
	ds_read_b128 v[176:179], v211 offset:0
	ds_read_b128 v[180:183], v211 offset:64
	v_mfma_f32_16x16x32_f16 v[164:167], v[68:71], v[132:135], v[164:167]
	v_mfma_f32_16x16x32_f16 v[160:163], v[60:63], v[140:143], v[160:163]
	global_load_dwordx4 v[144:147], v[228:229], off offset:0
	global_load_dwordx4 v[148:151], v[228:229], off offset:64
	global_load_dwordx4 v[152:155], v[228:229], off offset:128
	global_load_dwordx4 v[156:159], v[228:229], off offset:192
	v_lshl_add_u64 v[228:229], v[228:229], 0, s[20:21]
	s_waitcnt lgkmcnt(3)
	v_mfma_f32_16x16x32_f16 v[168:171], v[16:19], v[184:187], v[192:195]
	v_mfma_f32_16x16x32_f16 v[172:175], v[24:27], v[184:187], v[192:195]
	s_waitcnt lgkmcnt(2)
	v_mfma_f32_16x16x32_f16 v[168:171], v[20:23], v[188:191], v[168:171]
	v_mfma_f32_16x16x32_f16 v[172:175], v[28:31], v[188:191], v[172:175]
	s_waitcnt lgkmcnt(1)
	v_mfma_f32_16x16x32_f16 v[168:171], v[32:35], v[176:179], v[168:171]
	v_mfma_f32_16x16x32_f16 v[172:175], v[40:43], v[176:179], v[172:175]
	s_waitcnt lgkmcnt(0)
	v_mfma_f32_16x16x32_f16 v[168:171], v[36:39], v[180:183], v[168:171]
	v_mfma_f32_16x16x32_f16 v[172:175], v[44:47], v[180:183], v[172:175]
	v_max_f32_e32 v221, v221, v215
	s_nop 6
	v_mov_b32_dpp v168, v172 quad_perm:[0,1,2,3] row_mask:0xf bank_mask:0xa
	v_mov_b32_dpp v169, v173 quad_perm:[0,1,2,3] row_mask:0xf bank_mask:0xa
	v_mov_b32_dpp v170, v174 quad_perm:[0,1,2,3] row_mask:0xf bank_mask:0xa
	v_exp_f32_e32 v200, v168
	v_mov_b32_dpp v171, v175 quad_perm:[0,1,2,3] row_mask:0xf bank_mask:0xa
	v_exp_f32_e32 v201, v169
	v_exp_f32_e32 v202, v170
	v_add_f32_e32 v200, 1.0, v200
	v_exp_f32_e32 v203, v171
	v_add_f32_e32 v201, 1.0, v201
	v_add_f32_e32 v202, 1.0, v202
	v_rcp_f32_e32 v202, v202
	v_rcp_f32_e32 v200, v200
	v_rcp_f32_e32 v201, v201
	v_add_f32_e32 v203, 1.0, v203
	v_fmamk_f32 v204, v202, 0xc0b8aa3b, v222
	v_rcp_f32_e32 v203, v203
	v_mul_f32_e32 v205, v200, v204
	v_fma_f32 v220, v201, v220, v205
	v_exp_f32_e32 v206, v220
	v_mul_f32_e32 v207, -2.0, v203
	v_add_f32_e32 v206, 1.0, v206
	v_rcp_f32_e32 v206, v206
	s_nop 0
	v_fma_mixlo_f16 v208, v206, v207, v203
	ds_write_b16 v225, v208 offset:576
	v_fma_f32 v215, v206, v207, v203
	v_mfma_f32_16x16x32_f16 v[232:235], v[80:83], v[128:131], v[120:123]
	v_mfma_f32_16x16x32_f16 v[164:167], v[72:75], v[136:139], v[164:167]
	ds_write_b128 v227, v[160:163] offset:0
	ds_read_b128 v[196:199], v226 offset:5440
	s_waitcnt lgkmcnt(2)
	s_barrier
	ds_read_b128 v[184:187], v210 offset:576
	ds_read_b128 v[188:191], v210 offset:640
	ds_read_b128 v[176:179], v212 offset:576
	ds_read_b128 v[180:183], v212 offset:640
	v_mfma_f32_16x16x32_f16 v[232:235], v[84:87], v[132:135], v[232:235]
	v_mfma_f32_16x16x32_f16 v[164:167], v[76:79], v[140:143], v[164:167]
	s_waitcnt lgkmcnt(3)
	v_mfma_f32_16x16x32_f16 v[168:171], v[16:19], v[184:187], v[196:199]
	v_mfma_f32_16x16x32_f16 v[172:175], v[24:27], v[184:187], v[196:199]
	s_waitcnt lgkmcnt(2)
	v_mfma_f32_16x16x32_f16 v[168:171], v[20:23], v[188:191], v[168:171]
	v_mfma_f32_16x16x32_f16 v[172:175], v[28:31], v[188:191], v[172:175]
	s_waitcnt lgkmcnt(1)
	v_mfma_f32_16x16x32_f16 v[168:171], v[32:35], v[176:179], v[168:171]
	v_mfma_f32_16x16x32_f16 v[172:175], v[40:43], v[176:179], v[172:175]
	s_waitcnt lgkmcnt(0)
	v_mfma_f32_16x16x32_f16 v[168:171], v[36:39], v[180:183], v[168:171]
	v_mfma_f32_16x16x32_f16 v[172:175], v[44:47], v[180:183], v[172:175]
	v_max_f32_e32 v221, v221, v215
	s_nop 6
	v_mov_b32_dpp v168, v172 quad_perm:[0,1,2,3] row_mask:0xf bank_mask:0xa
	v_mov_b32_dpp v169, v173 quad_perm:[0,1,2,3] row_mask:0xf bank_mask:0xa
	v_mov_b32_dpp v170, v174 quad_perm:[0,1,2,3] row_mask:0xf bank_mask:0xa
	v_exp_f32_e32 v200, v168
	v_mov_b32_dpp v171, v175 quad_perm:[0,1,2,3] row_mask:0xf bank_mask:0xa
	v_exp_f32_e32 v201, v169
	v_exp_f32_e32 v202, v170
	v_add_f32_e32 v200, 1.0, v200
	v_exp_f32_e32 v203, v171
	v_add_f32_e32 v201, 1.0, v201
	v_add_f32_e32 v202, 1.0, v202
	v_rcp_f32_e32 v202, v202
	v_rcp_f32_e32 v200, v200
	v_rcp_f32_e32 v201, v201
	v_add_f32_e32 v203, 1.0, v203
	v_fmamk_f32 v204, v202, 0xc0b8aa3b, v222
	v_rcp_f32_e32 v203, v203
	v_mul_f32_e32 v205, v200, v204
	v_fma_f32 v220, v201, v220, v205
	v_exp_f32_e32 v206, v220
	v_mul_f32_e32 v207, -2.0, v203
	v_add_f32_e32 v206, 1.0, v206
	v_rcp_f32_e32 v206, v206
	s_nop 0
	v_fma_mixlo_f16 v208, v206, v207, v203
	ds_write_b16 v225, v208 offset:0
	v_fma_f32 v215, v206, v207, v203
	v_mfma_f32_16x16x32_f16 v[236:239], v[96:99], v[128:131], v[124:127]
	v_mfma_f32_16x16x32_f16 v[232:235], v[88:91], v[136:139], v[232:235]
	ds_write_b128 v227, v[164:167] offset:64
	ds_read_b128 v[192:195], v226 offset:6528
	s_waitcnt lgkmcnt(2)
	s_barrier
	ds_read_b128 v[184:187], v209 offset:0
	ds_read_b128 v[188:191], v209 offset:64
	ds_read_b128 v[176:179], v211 offset:0
	ds_read_b128 v[180:183], v211 offset:64
	v_mfma_f32_16x16x32_f16 v[236:239], v[100:103], v[132:135], v[236:239]
	v_mfma_f32_16x16x32_f16 v[232:235], v[92:95], v[140:143], v[232:235]
	s_waitcnt lgkmcnt(3)
	v_mfma_f32_16x16x32_f16 v[168:171], v[16:19], v[184:187], v[192:195]
	v_mfma_f32_16x16x32_f16 v[172:175], v[24:27], v[184:187], v[192:195]
	s_waitcnt lgkmcnt(2)
	v_mfma_f32_16x16x32_f16 v[168:171], v[20:23], v[188:191], v[168:171]
	v_mfma_f32_16x16x32_f16 v[172:175], v[28:31], v[188:191], v[172:175]
	s_waitcnt lgkmcnt(1)
	v_mfma_f32_16x16x32_f16 v[168:171], v[32:35], v[176:179], v[168:171]
	v_mfma_f32_16x16x32_f16 v[172:175], v[40:43], v[176:179], v[172:175]
	s_waitcnt lgkmcnt(0)
	v_mfma_f32_16x16x32_f16 v[168:171], v[36:39], v[180:183], v[168:171]
	v_mfma_f32_16x16x32_f16 v[172:175], v[44:47], v[180:183], v[172:175]
	v_max_f32_e32 v221, v221, v215
	s_nop 6
	v_mov_b32_dpp v168, v172 quad_perm:[0,1,2,3] row_mask:0xf bank_mask:0xa
	v_mov_b32_dpp v169, v173 quad_perm:[0,1,2,3] row_mask:0xf bank_mask:0xa
	v_mov_b32_dpp v170, v174 quad_perm:[0,1,2,3] row_mask:0xf bank_mask:0xa
	v_exp_f32_e32 v200, v168
	v_mov_b32_dpp v171, v175 quad_perm:[0,1,2,3] row_mask:0xf bank_mask:0xa
	v_exp_f32_e32 v201, v169
	v_exp_f32_e32 v202, v170
	v_add_f32_e32 v200, 1.0, v200
	v_exp_f32_e32 v203, v171
	v_add_f32_e32 v201, 1.0, v201
	v_add_f32_e32 v202, 1.0, v202
	v_rcp_f32_e32 v202, v202
	v_rcp_f32_e32 v200, v200
	v_rcp_f32_e32 v201, v201
	v_add_f32_e32 v203, 1.0, v203
	v_fmamk_f32 v204, v202, 0xc0b8aa3b, v222
	v_rcp_f32_e32 v203, v203
	v_mul_f32_e32 v205, v200, v204
	v_fma_f32 v220, v201, v220, v205
	v_exp_f32_e32 v206, v220
	v_mul_f32_e32 v207, -2.0, v203
	v_add_f32_e32 v206, 1.0, v206
	v_rcp_f32_e32 v206, v206
	s_nop 0
	v_fma_mixlo_f16 v208, v206, v207, v203
	ds_write_b16 v225, v208 offset:576
	v_fma_f32 v215, v206, v207, v203
	s_waitcnt vmcnt(0)
	v_mfma_f32_16x16x32_f16 v[160:163], v[48:51], v[144:147], v[112:115]
	v_mfma_f32_16x16x32_f16 v[236:239], v[104:107], v[136:139], v[236:239]
	ds_write_b128 v227, v[232:235] offset:128
	ds_read_b128 v[196:199], v226 offset:7616
	s_waitcnt lgkmcnt(2)
	s_barrier
	ds_read_b128 v[184:187], v210 offset:576
	ds_read_b128 v[188:191], v210 offset:640
	ds_read_b128 v[176:179], v212 offset:576
	ds_read_b128 v[180:183], v212 offset:640
	v_mfma_f32_16x16x32_f16 v[160:163], v[52:55], v[148:151], v[160:163]
	v_mfma_f32_16x16x32_f16 v[236:239], v[108:111], v[140:143], v[236:239]
	s_waitcnt lgkmcnt(3)
	v_mfma_f32_16x16x32_f16 v[168:171], v[16:19], v[184:187], v[196:199]
	v_mfma_f32_16x16x32_f16 v[172:175], v[24:27], v[184:187], v[196:199]
	s_waitcnt lgkmcnt(2)
	v_mfma_f32_16x16x32_f16 v[168:171], v[20:23], v[188:191], v[168:171]
	v_mfma_f32_16x16x32_f16 v[172:175], v[28:31], v[188:191], v[172:175]
	s_waitcnt lgkmcnt(1)
	v_mfma_f32_16x16x32_f16 v[168:171], v[32:35], v[176:179], v[168:171]
	v_mfma_f32_16x16x32_f16 v[172:175], v[40:43], v[176:179], v[172:175]
	s_waitcnt lgkmcnt(0)
	v_mfma_f32_16x16x32_f16 v[168:171], v[36:39], v[180:183], v[168:171]
	v_mfma_f32_16x16x32_f16 v[172:175], v[44:47], v[180:183], v[172:175]
	v_max_f32_e32 v221, v221, v215
	s_nop 6
	v_mov_b32_dpp v168, v172 quad_perm:[0,1,2,3] row_mask:0xf bank_mask:0xa
	v_mov_b32_dpp v169, v173 quad_perm:[0,1,2,3] row_mask:0xf bank_mask:0xa
	v_mov_b32_dpp v170, v174 quad_perm:[0,1,2,3] row_mask:0xf bank_mask:0xa
	v_exp_f32_e32 v200, v168
	v_mov_b32_dpp v171, v175 quad_perm:[0,1,2,3] row_mask:0xf bank_mask:0xa
	v_exp_f32_e32 v201, v169
	v_exp_f32_e32 v202, v170
	v_add_f32_e32 v200, 1.0, v200
	v_exp_f32_e32 v203, v171
	v_add_f32_e32 v201, 1.0, v201
	v_add_f32_e32 v202, 1.0, v202
	v_rcp_f32_e32 v202, v202
	v_rcp_f32_e32 v200, v200
	v_rcp_f32_e32 v201, v201
	v_add_f32_e32 v203, 1.0, v203
	v_fmamk_f32 v204, v202, 0xc0b8aa3b, v222
	v_rcp_f32_e32 v203, v203
	v_mul_f32_e32 v205, v200, v204
	v_fma_f32 v220, v201, v220, v205
	v_exp_f32_e32 v206, v220
	v_mul_f32_e32 v207, -2.0, v203
	v_add_f32_e32 v206, 1.0, v206
	v_rcp_f32_e32 v206, v206
	s_nop 0
	v_fma_mixlo_f16 v208, v206, v207, v203
	ds_write_b16 v225, v208 offset:0
	v_fma_f32 v215, v206, v207, v203
	v_mfma_f32_16x16x32_f16 v[164:167], v[64:67], v[144:147], v[116:119]
	v_mfma_f32_16x16x32_f16 v[160:163], v[56:59], v[152:155], v[160:163]
	ds_write_b128 v227, v[236:239] offset:192
	ds_read_b128 v[192:195], v226 offset:0
	s_waitcnt lgkmcnt(2)
	s_barrier
	s_sub_u32 s4, s4, 1
	s_cmp_lg_u32 s4, 0
	s_cbranch_scc1 .Llstm3_loop
	v_max_f32_e32 v221, v221, v215
	global_store_dword v230, v221, s[12:13]
	s_endpgm
